# plus OUT epilogue: 16 residual loads issued up front (vmcnt(15) per chunk); MERGE epilogue wait relaxed to vmcnt(8)
# speedup vs baseline: 1.0072x; 1.0072x over previous
; __device__ __forceinline__ unsigned cvt_pk_bf16(float lo, float hi) { f32x2 v = {lo, hi}; bf16x2_t b = __builtin_convertvector(v, bf16x2_t); return __builtin_bit_cast(unsigned, b); }
;     __device__ __forceinline__ void operator()(const f32x4 (&acc)[2][2][4][2], f32x4 (&tot)[2][4][2], const u32x2 (&pf)[8], const g8::Unit& u, int wr, int wc, int fr, int fq) const {
;         const int br = u.tag & 3, row0 = u.pm * 256 + wr * 64 + fr, col0 = u.pn * 256 + (u.tag >> 2) * 128 + wc * 32 + 8 * fq;
; #pragma unroll
;         for (int ai = 0; ai < 2; ++ai)
; #pragma unroll
;             for (int m = 0; m < 4; ++m) { const int row = row0 + ai * 128 + m * 16;
;                 const u32x2 g = pf[ai * 4 + m];
;                 const f32x4 g0 = {(float)(g.x & 0xffu), (float)((g.x >> 8) & 0xffu), (float)((g.x >> 16) & 0xffu), (float)(g.x >> 24)};
;                 const f32x4 g1 = {(float)(g.y & 0xffu), (float)((g.y >> 8) & 0xffu), (float)((g.y >> 16) & 0xffu), (float)(g.y >> 24)};
;                 const f32x4 t0 = g0 * acc[ai][0][m][0], t1 = g1 * acc[ai][0][m][1];
;                 if (br == 0) { tot[ai][m][0] = t0; tot[ai][m][1] = t1; } else { tot[ai][m][0] += t0; tot[ai][m][1] += t1; }
;                 if (br == 3) { const f32x4 s0 = tot[ai][m][0] * (1.f / 255.f), s1 = tot[ai][m][1] * (1.f / 255.f);
;                     u32x4 w; w.x = cvt_pk_bf16(s0[0], s0[1]); w.y = cvt_pk_bf16(s0[2], s0[3]); w.z = cvt_pk_bf16(s1[0], s1[1]); w.w = cvt_pk_bf16(s1[2], s1[3]);
;                     *(u32x4*)(MG + (size_t)row * 1024 + col0) = w; } }
;     }
.LBB0_1193:
	s_mov_b32 s42, -1
	s_lshl_b32 s43, s61, 5
	s_and_b32 s43, s43, 0xffffff80
	v_mbcnt_lo_u32_b32 v1, s42, 0
	v_mbcnt_hi_u32_b32 v1, s42, v1
	s_lshl_b32 s42, s60, 8
	s_or_b32 s43, s43, s95
	s_and_b32 s44, s61, 3
	v_lshrrev_b32_e32 v149, 1, v1
	s_add_i32 s43, s43, s42
	s_waitcnt vmcnt(8)
	v_cvt_f32_ubyte3_e32 v151, v167
	v_cvt_f32_ubyte2_e32 v150, v167
	v_and_b32_e32 v149, 56, v149
	s_cmp_eq_u32 s44, 0
	v_pk_mul_f32 v[152:153], v[62:63], v[150:151]
	v_pk_fma_f32 v[62:63], v[62:63], v[150:151], v[142:143]
	v_cvt_f32_ubyte1_e32 v143, v166
	v_cvt_f32_ubyte0_e32 v142, v166
	v_cvt_f32_ubyte3_e32 v151, v166
	v_cvt_f32_ubyte2_e32 v150, v166
	v_cvt_f32_ubyte1_e32 v155, v167
	v_cvt_f32_ubyte0_e32 v154, v167
	v_add_u32_e32 v168, s43, v149
	v_and_or_b32 v1, v1, 15, s9
	s_cselect_b64 s[42:43], -1, 0
	s_cmp_eq_u32 s44, 3
	v_pk_mul_f32 v[166:167], v[66:67], v[150:151]
	v_pk_mul_f32 v[172:173], v[64:65], v[142:143]
	v_pk_mul_f32 v[174:175], v[60:61], v[154:155]
	v_pk_fma_f32 v[66:67], v[66:67], v[150:151], v[140:141]
	v_pk_fma_f32 v[64:65], v[64:65], v[142:143], v[138:139]
	v_pk_fma_f32 v[60:61], v[60:61], v[154:155], v[130:131]
	v_lshl_add_u32 v170, s4, 8, v1
	s_cselect_b64 s[46:47], -1, 0
	s_cmp_lg_u32 s44, 3
	v_ashrrev_i32_e32 v169, 31, v168
	v_cndmask_b32_e64 v143, v63, v153, s[42:43]
	v_cndmask_b32_e64 v142, v62, v152, s[42:43]
	v_cndmask_b32_e64 v131, v61, v175, s[42:43]
	v_cndmask_b32_e64 v130, v60, v174, s[42:43]
	v_cndmask_b32_e64 v141, v67, v167, s[42:43]
	v_cndmask_b32_e64 v140, v66, v166, s[42:43]
	v_cndmask_b32_e64 v139, v65, v173, s[42:43]
	v_cndmask_b32_e64 v138, v64, v172, s[42:43]
	s_cbranch_scc1 .LBB0_1195
	s_mov_b32 s4, 0x3b808081
	v_pk_mul_f32 v[62:63], v[140:141], s[4:5] op_sel_hi:[1,0]
	v_pk_mul_f32 v[60:61], v[138:139], s[4:5] op_sel_hi:[1,0]
	v_pk_mul_f32 v[64:65], v[142:143], s[4:5] op_sel_hi:[1,0]
	v_ashrrev_i32_e32 v171, 31, v170
	v_cvt_pk_bf16_f32 v60, v60, v61
	v_cvt_pk_bf16_f32 v61, v62, v63
	v_cvt_pk_bf16_f32 v63, v64, v65
	v_lshlrev_b64 v[64:65], 11, v[170:171]
	v_pk_mul_f32 v[66:67], v[130:131], s[4:5] op_sel_hi:[1,0]
	v_lshl_add_u64 v[64:65], s[14:15], 0, v[64:65]
	v_cvt_pk_bf16_f32 v62, v66, v67
	v_lshl_add_u64 v[64:65], v[168:169], 1, v[64:65]
	global_store_dwordx4 v[64:65], v[60:63], off

; __device__ __forceinline__ unsigned cvt_pk_bf16(float lo, float hi) { f32x2 v = {lo, hi}; bf16x2_t b = __builtin_convertvector(v, bf16x2_t); return __builtin_bit_cast(unsigned, b); }
;     __device__ __forceinline__ void operator()(const f32x4 (&acc)[2][2][4][2], const g8::Unit& u, int wr, int wc, int fr, int fq) const {
;         const int row0 = u.pm * 256 + wr * 64 + fr, col0 = u.pn * 256 + wc * 32 + 8 * fq;
; #pragma unroll
;         for (int ai = 0; ai < 2; ++ai)
; #pragma unroll
;             for (int m = 0; m < 4; ++m) { const size_t ro = (size_t)(row0 + ai * 128 + m * 16) * 1024;
; #pragma unroll
;                 for (int bj = 0; bj < 2; ++bj) { const size_t o = ro + col0 + bj * 128;
;                     const u32x4 xb = *(const u32x4*)(XBp + o);
;                     const f32x4 x0 = {__uint_as_float(xb.x << 16), __uint_as_float(xb.x & 0xffff0000u), __uint_as_float(xb.y << 16), __uint_as_float(xb.y & 0xffff0000u)};
;                     const f32x4 x1 = {__uint_as_float(xb.z << 16), __uint_as_float(xb.z & 0xffff0000u), __uint_as_float(xb.w << 16), __uint_as_float(xb.w & 0xffff0000u)};
;                     const f32x4 y0 = x0 * ALPHA + acc[ai][bj][m][0], y1 = x1 * ALPHA + acc[ai][bj][m][1];
;                     *(u32x4*)(Y + o) = (u32x4){cvt_pk_bf16(y0[0], y0[1]), cvt_pk_bf16(y0[2], y0[3]), cvt_pk_bf16(y1[0], y1[1]), cvt_pk_bf16(y1[2], y1[3])}; } }
;     }
.LBB0_1288:
	s_mov_b32 s42, -1
	s_andn2_b64 vcc, exec, s[40:41]
	v_mbcnt_lo_u32_b32 v1, s42, 0
	v_mbcnt_hi_u32_b32 v1, s42, v1
	s_lshl_b32 s42, s63, 8
	s_add_i32 s42, s42, s9
	v_and_or_b32 v156, v1, 15, s42
	s_lshl_b32 s42, s62, 8
	v_lshrrev_b32_e32 v1, 1, v1
	s_or_b32 s42, s42, s95
	v_and_b32_e32 v1, 56, v1
	v_add_u32_e32 v146, s42, v1
	v_ashrrev_i32_e32 v157, 31, v156
	v_ashrrev_i32_e32 v147, 31, v146
	v_lshlrev_b64 v[144:145], 10, v[156:157]
	v_lshl_add_u64 v[144:145], v[144:145], 0, v[146:147]
	v_lshlrev_b64 v[144:145], 1, v[144:145]
	v_lshl_add_u64 v[154:155], s[10:11], 0, v[144:145]
	global_load_dwordx4 v[162:165], v[154:155], off
	global_load_dwordx4 v[166:169], v[154:155], off offset:256
	s_mov_b64 s[42:43], 0x8000
	v_lshl_add_u64 v[236:237], v[154:155], 0, s[42:43]
	global_load_dwordx4 v[170:173], v[236:237], off
	global_load_dwordx4 v[174:177], v[236:237], off offset:256
	s_mov_b64 s[42:43], 0x10000
	v_lshl_add_u64 v[236:237], v[154:155], 0, s[42:43]
	global_load_dwordx4 v[178:181], v[236:237], off
	global_load_dwordx4 v[184:187], v[236:237], off offset:256
	s_mov_b64 s[42:43], 0x18000
	v_lshl_add_u64 v[236:237], v[154:155], 0, s[42:43]
	global_load_dwordx4 v[188:191], v[236:237], off
	global_load_dwordx4 v[192:195], v[236:237], off offset:256
	s_mov_b64 s[42:43], 0x40000
	v_lshl_add_u64 v[236:237], v[154:155], 0, s[42:43]
	global_load_dwordx4 v[196:199], v[236:237], off
	global_load_dwordx4 v[206:209], v[236:237], off offset:256
	s_mov_b64 s[42:43], 0x48000
	v_lshl_add_u64 v[236:237], v[154:155], 0, s[42:43]
	global_load_dwordx4 v[210:213], v[236:237], off
	global_load_dwordx4 v[214:217], v[236:237], off offset:256
	s_mov_b64 s[42:43], 0x50000
	v_lshl_add_u64 v[236:237], v[154:155], 0, s[42:43]
	global_load_dwordx4 v[218:221], v[236:237], off
	global_load_dwordx4 v[222:225], v[236:237], off offset:256
	s_mov_b64 s[42:43], 0x58000
	v_lshl_add_u64 v[236:237], v[154:155], 0, s[42:43]
	global_load_dwordx4 v[228:231], v[236:237], off
	global_load_dwordx4 v[232:235], v[236:237], off offset:256
	s_mov_b64 s[42:43], 0x40000
	s_waitcnt vmcnt(15)
	v_lshlrev_b32_e32 v158, 16, v162
	v_and_b32_e32 v159, 0xffff0000, v162
	v_lshlrev_b32_e32 v150, 16, v163
	v_and_b32_e32 v151, 0xffff0000, v163
	v_lshlrev_b32_e32 v160, 16, v164
	v_and_b32_e32 v161, 0xffff0000, v164
	v_lshlrev_b32_e32 v152, 16, v165
	v_and_b32_e32 v153, 0xffff0000, v165
	v_pk_fma_f32 v[130:131], v[150:151], s[24:25], v[130:131] op_sel_hi:[1,0,1]
	v_pk_fma_f32 v[128:129], v[158:159], s[24:25], v[128:129] op_sel_hi:[1,0,1]
	v_pk_fma_f32 v[150:151], v[152:153], s[24:25], v[126:127] op_sel_hi:[1,0,1]
	v_pk_fma_f32 v[126:127], v[160:161], s[24:25], v[124:125] op_sel_hi:[1,0,1]
	v_cvt_pk_bf16_f32 v124, v128, v129
	v_cvt_pk_bf16_f32 v125, v130, v131
	v_cvt_pk_bf16_f32 v126, v126, v127
	v_cvt_pk_bf16_f32 v127, v150, v151
	v_lshl_add_u64 v[128:129], s[14:15], 0, v[144:145]
	global_store_dwordx4 v[128:129], v[124:127], off
	s_waitcnt vmcnt(15)
	v_lshlrev_b32_e32 v130, 16, v166
	v_and_b32_e32 v131, 0xffff0000, v166
	v_lshlrev_b32_e32 v124, 16, v167
	v_and_b32_e32 v125, 0xffff0000, v167
	v_lshlrev_b32_e32 v150, 16, v168
	v_and_b32_e32 v151, 0xffff0000, v168
	v_lshlrev_b32_e32 v126, 16, v169
	v_and_b32_e32 v127, 0xffff0000, v169
	v_pk_fma_f32 v[122:123], v[124:125], s[24:25], v[122:123] op_sel_hi:[1,0,1]
	v_pk_fma_f32 v[120:121], v[130:131], s[24:25], v[120:121] op_sel_hi:[1,0,1]
	v_pk_fma_f32 v[124:125], v[126:127], s[24:25], v[118:119] op_sel_hi:[1,0,1]
	v_pk_fma_f32 v[118:119], v[150:151], s[24:25], v[116:117] op_sel_hi:[1,0,1]
	v_cvt_pk_bf16_f32 v116, v120, v121
	v_cvt_pk_bf16_f32 v117, v122, v123
	v_cvt_pk_bf16_f32 v118, v118, v119
	v_cvt_pk_bf16_f32 v119, v124, v125
	global_store_dwordx4 v[128:129], v[116:119], off offset:256
	s_nop 1
	v_or_b32_e32 v116, 16, v156
	v_ashrrev_i32_e32 v117, 31, v116
	v_lshlrev_b64 v[116:117], 10, v[116:117]
	v_lshl_add_u64 v[116:117], v[116:117], 0, v[146:147]
	v_lshlrev_b64 v[120:121], 1, v[116:117]
	v_lshl_add_u64 v[122:123], s[10:11], 0, v[120:121]
	s_waitcnt vmcnt(15)
	v_lshlrev_b32_e32 v124, 16, v170
	v_and_b32_e32 v125, 0xffff0000, v170
	v_lshlrev_b32_e32 v116, 16, v171
	v_and_b32_e32 v117, 0xffff0000, v171
	v_lshlrev_b32_e32 v126, 16, v172
	v_and_b32_e32 v127, 0xffff0000, v172
	v_lshlrev_b32_e32 v118, 16, v173
	v_and_b32_e32 v119, 0xffff0000, v173
	v_pk_fma_f32 v[114:115], v[116:117], s[24:25], v[114:115] op_sel_hi:[1,0,1]
	v_pk_fma_f32 v[112:113], v[124:125], s[24:25], v[112:113] op_sel_hi:[1,0,1]
	v_pk_fma_f32 v[116:117], v[118:119], s[24:25], v[110:111] op_sel_hi:[1,0,1]
	v_pk_fma_f32 v[110:111], v[126:127], s[24:25], v[108:109] op_sel_hi:[1,0,1]
	v_cvt_pk_bf16_f32 v108, v112, v113
	v_cvt_pk_bf16_f32 v109, v114, v115
	v_cvt_pk_bf16_f32 v110, v110, v111
	v_cvt_pk_bf16_f32 v111, v116, v117
	v_lshl_add_u64 v[112:113], s[14:15], 0, v[120:121]
	global_store_dwordx4 v[112:113], v[108:111], off
	s_waitcnt vmcnt(15)
	v_lshlrev_b32_e32 v114, 16, v174
	v_and_b32_e32 v115, 0xffff0000, v174
	v_lshlrev_b32_e32 v108, 16, v175
	v_and_b32_e32 v109, 0xffff0000, v175
	v_lshlrev_b32_e32 v116, 16, v176
	v_and_b32_e32 v117, 0xffff0000, v176
	v_lshlrev_b32_e32 v110, 16, v177
	v_and_b32_e32 v111, 0xffff0000, v177
	v_pk_fma_f32 v[106:107], v[108:109], s[24:25], v[106:107] op_sel_hi:[1,0,1]
	v_pk_fma_f32 v[104:105], v[114:115], s[24:25], v[104:105] op_sel_hi:[1,0,1]
	v_pk_fma_f32 v[108:109], v[110:111], s[24:25], v[102:103] op_sel_hi:[1,0,1]
	v_pk_fma_f32 v[102:103], v[116:117], s[24:25], v[100:101] op_sel_hi:[1,0,1]
	v_cvt_pk_bf16_f32 v100, v104, v105
	v_cvt_pk_bf16_f32 v101, v106, v107
	v_cvt_pk_bf16_f32 v102, v102, v103
	v_cvt_pk_bf16_f32 v103, v108, v109
	global_store_dwordx4 v[112:113], v[100:103], off offset:256
	s_nop 1
	v_or_b32_e32 v100, 32, v156
	v_ashrrev_i32_e32 v101, 31, v100
	v_lshlrev_b64 v[100:101], 10, v[100:101]
	v_lshl_add_u64 v[100:101], v[100:101], 0, v[146:147]
	v_lshlrev_b64 v[104:105], 1, v[100:101]
	v_lshl_add_u64 v[106:107], s[10:11], 0, v[104:105]
	s_waitcnt vmcnt(15)
; __device__ __forceinline__ unsigned cvt_pk_bf16(float lo, float hi) { f32x2 v = {lo, hi}; bf16x2_t b = __builtin_convertvector(v, bf16x2_t); return __builtin_bit_cast(unsigned, b); }
;     __device__ __forceinline__ void operator()(const f32x4 (&acc)[2][2][4][2], const g8::Unit& u, int wr, int wc, int fr, int fq) const {
;         const int row0 = u.pm * 256 + wr * 64 + fr, col0 = u.pn * 256 + wc * 32 + 8 * fq;
; #pragma unroll
;         for (int ai = 0; ai < 2; ++ai)
; #pragma unroll
;             for (int m = 0; m < 4; ++m) { const size_t ro = (size_t)(row0 + ai * 128 + m * 16) * 1024;
; #pragma unroll
;                 for (int bj = 0; bj < 2; ++bj) { const size_t o = ro + col0 + bj * 128;
;                     const u32x4 xb = *(const u32x4*)(XBp + o);
;                     const f32x4 x0 = {__uint_as_float(xb.x << 16), __uint_as_float(xb.x & 0xffff0000u), __uint_as_float(xb.y << 16), __uint_as_float(xb.y & 0xffff0000u)};
;                     const f32x4 x1 = {__uint_as_float(xb.z << 16), __uint_as_float(xb.z & 0xffff0000u), __uint_as_float(xb.w << 16), __uint_as_float(xb.w & 0xffff0000u)};
;                     const f32x4 y0 = x0 * ALPHA + acc[ai][bj][m][0], y1 = x1 * ALPHA + acc[ai][bj][m][1];
;                     *(u32x4*)(Y + o) = (u32x4){cvt_pk_bf16(y0[0], y0[1]), cvt_pk_bf16(y0[2], y0[3]), cvt_pk_bf16(y1[0], y1[1]), cvt_pk_bf16(y1[2], y1[3])}; } }
;     }
	v_lshlrev_b32_e32 v108, 16, v178
	v_and_b32_e32 v109, 0xffff0000, v178
	v_lshlrev_b32_e32 v100, 16, v179
	v_and_b32_e32 v101, 0xffff0000, v179
	v_lshlrev_b32_e32 v110, 16, v180
	v_and_b32_e32 v111, 0xffff0000, v180
	v_lshlrev_b32_e32 v102, 16, v181
	v_and_b32_e32 v103, 0xffff0000, v181
	v_pk_fma_f32 v[98:99], v[100:101], s[24:25], v[98:99] op_sel_hi:[1,0,1]
	v_pk_fma_f32 v[96:97], v[108:109], s[24:25], v[96:97] op_sel_hi:[1,0,1]
	v_pk_fma_f32 v[100:101], v[102:103], s[24:25], v[94:95] op_sel_hi:[1,0,1]
	v_pk_fma_f32 v[94:95], v[110:111], s[24:25], v[92:93] op_sel_hi:[1,0,1]
	v_cvt_pk_bf16_f32 v92, v96, v97
	v_cvt_pk_bf16_f32 v93, v98, v99
	v_cvt_pk_bf16_f32 v94, v94, v95
	v_cvt_pk_bf16_f32 v95, v100, v101
	v_lshl_add_u64 v[96:97], s[14:15], 0, v[104:105]
	global_store_dwordx4 v[96:97], v[92:95], off
	s_waitcnt vmcnt(15)
	v_lshlrev_b32_e32 v98, 16, v184
	v_and_b32_e32 v99, 0xffff0000, v184
	v_lshlrev_b32_e32 v92, 16, v185
	v_and_b32_e32 v93, 0xffff0000, v185
	v_lshlrev_b32_e32 v100, 16, v186
	v_and_b32_e32 v101, 0xffff0000, v186
	v_lshlrev_b32_e32 v94, 16, v187
	v_and_b32_e32 v95, 0xffff0000, v187
	v_pk_fma_f32 v[90:91], v[92:93], s[24:25], v[90:91] op_sel_hi:[1,0,1]
	v_pk_fma_f32 v[88:89], v[98:99], s[24:25], v[88:89] op_sel_hi:[1,0,1]
	v_pk_fma_f32 v[92:93], v[94:95], s[24:25], v[86:87] op_sel_hi:[1,0,1]
	v_pk_fma_f32 v[86:87], v[100:101], s[24:25], v[84:85] op_sel_hi:[1,0,1]
	v_cvt_pk_bf16_f32 v84, v88, v89
	v_cvt_pk_bf16_f32 v85, v90, v91
	v_cvt_pk_bf16_f32 v86, v86, v87
	v_cvt_pk_bf16_f32 v87, v92, v93
	global_store_dwordx4 v[96:97], v[84:87], off offset:256
	s_nop 1
	v_or_b32_e32 v84, 48, v156
	v_ashrrev_i32_e32 v85, 31, v84
	v_lshlrev_b64 v[84:85], 10, v[84:85]
	v_lshl_add_u64 v[84:85], v[84:85], 0, v[146:147]
	v_lshlrev_b64 v[88:89], 1, v[84:85]
	v_lshl_add_u64 v[90:91], s[10:11], 0, v[88:89]
	s_waitcnt vmcnt(15)
	v_lshlrev_b32_e32 v92, 16, v188
	v_and_b32_e32 v93, 0xffff0000, v188
	v_lshlrev_b32_e32 v84, 16, v189
	v_and_b32_e32 v85, 0xffff0000, v189
	v_lshlrev_b32_e32 v94, 16, v190
	v_and_b32_e32 v95, 0xffff0000, v190
	v_lshlrev_b32_e32 v86, 16, v191
	v_and_b32_e32 v87, 0xffff0000, v191
	v_pk_fma_f32 v[82:83], v[84:85], s[24:25], v[82:83] op_sel_hi:[1,0,1]
	v_pk_fma_f32 v[80:81], v[92:93], s[24:25], v[80:81] op_sel_hi:[1,0,1]
	v_pk_fma_f32 v[84:85], v[86:87], s[24:25], v[78:79] op_sel_hi:[1,0,1]
	v_pk_fma_f32 v[78:79], v[94:95], s[24:25], v[76:77] op_sel_hi:[1,0,1]
	v_cvt_pk_bf16_f32 v76, v80, v81
	v_cvt_pk_bf16_f32 v77, v82, v83
	v_cvt_pk_bf16_f32 v78, v78, v79
	v_cvt_pk_bf16_f32 v79, v84, v85
	v_lshl_add_u64 v[80:81], s[14:15], 0, v[88:89]
	global_store_dwordx4 v[80:81], v[76:79], off
	s_waitcnt vmcnt(15)
	v_lshlrev_b32_e32 v82, 16, v192
	v_and_b32_e32 v83, 0xffff0000, v192
	v_lshlrev_b32_e32 v76, 16, v193
	v_and_b32_e32 v77, 0xffff0000, v193
	v_lshlrev_b32_e32 v84, 16, v194
	v_and_b32_e32 v85, 0xffff0000, v194
	v_lshlrev_b32_e32 v78, 16, v195
	v_and_b32_e32 v79, 0xffff0000, v195
	v_pk_fma_f32 v[74:75], v[76:77], s[24:25], v[74:75] op_sel_hi:[1,0,1]
	v_pk_fma_f32 v[72:73], v[82:83], s[24:25], v[72:73] op_sel_hi:[1,0,1]
	v_pk_fma_f32 v[76:77], v[78:79], s[24:25], v[70:71] op_sel_hi:[1,0,1]
	v_pk_fma_f32 v[70:71], v[84:85], s[24:25], v[68:69] op_sel_hi:[1,0,1]
	v_cvt_pk_bf16_f32 v68, v72, v73
	v_cvt_pk_bf16_f32 v69, v74, v75
	v_cvt_pk_bf16_f32 v70, v70, v71
	v_cvt_pk_bf16_f32 v71, v76, v77
	v_lshl_add_u64 v[72:73], v[144:145], 0, s[42:43]
	global_store_dwordx4 v[80:81], v[68:71], off offset:256
	v_lshl_add_u64 v[74:75], s[10:11], 0, v[72:73]
	s_mov_b64 s[42:43], 0x48000
	s_waitcnt vmcnt(15)
	v_lshlrev_b32_e32 v76, 16, v196
	v_and_b32_e32 v77, 0xffff0000, v196
	v_lshlrev_b32_e32 v68, 16, v197
	v_and_b32_e32 v69, 0xffff0000, v197
	v_lshlrev_b32_e32 v78, 16, v198
	v_and_b32_e32 v79, 0xffff0000, v198
	v_lshlrev_b32_e32 v70, 16, v199
	v_and_b32_e32 v71, 0xffff0000, v199
	v_pk_fma_f32 v[66:67], v[68:69], s[24:25], v[66:67] op_sel_hi:[1,0,1]
	v_pk_fma_f32 v[64:65], v[76:77], s[24:25], v[64:65] op_sel_hi:[1,0,1]
	v_pk_fma_f32 v[68:69], v[70:71], s[24:25], v[62:63] op_sel_hi:[1,0,1]
	v_pk_fma_f32 v[62:63], v[78:79], s[24:25], v[60:61] op_sel_hi:[1,0,1]
	v_cvt_pk_bf16_f32 v60, v64, v65
	v_cvt_pk_bf16_f32 v61, v66, v67
	v_cvt_pk_bf16_f32 v62, v62, v63
	v_cvt_pk_bf16_f32 v63, v68, v69
	v_lshl_add_u64 v[64:65], s[14:15], 0, v[72:73]
	global_store_dwordx4 v[64:65], v[60:63], off
	s_waitcnt vmcnt(15)
	v_lshlrev_b32_e32 v66, 16, v206
	v_and_b32_e32 v67, 0xffff0000, v206
	v_lshlrev_b32_e32 v60, 16, v207
	v_and_b32_e32 v61, 0xffff0000, v207
	v_lshlrev_b32_e32 v68, 16, v208
	v_and_b32_e32 v69, 0xffff0000, v208
	v_lshlrev_b32_e32 v62, 16, v209
	v_and_b32_e32 v63, 0xffff0000, v209
	v_pk_fma_f32 v[58:59], v[60:61], s[24:25], v[58:59] op_sel_hi:[1,0,1]
	v_pk_fma_f32 v[56:57], v[66:67], s[24:25], v[56:57] op_sel_hi:[1,0,1]
	v_pk_fma_f32 v[60:61], v[62:63], s[24:25], v[54:55] op_sel_hi:[1,0,1]
	v_pk_fma_f32 v[54:55], v[68:69], s[24:25], v[52:53] op_sel_hi:[1,0,1]
	v_cvt_pk_bf16_f32 v52, v56, v57
	v_cvt_pk_bf16_f32 v53, v58, v59
	v_cvt_pk_bf16_f32 v54, v54, v55
	v_cvt_pk_bf16_f32 v55, v60, v61
	v_lshl_add_u64 v[56:57], v[144:145], 0, s[42:43]
	global_store_dwordx4 v[64:65], v[52:55], off offset:256
	v_lshl_add_u64 v[58:59], s[10:11], 0, v[56:57]
	s_mov_b64 s[42:43], 0x50000
	s_waitcnt vmcnt(15)
; __device__ __forceinline__ unsigned cvt_pk_bf16(float lo, float hi) { f32x2 v = {lo, hi}; bf16x2_t b = __builtin_convertvector(v, bf16x2_t); return __builtin_bit_cast(unsigned, b); }
;     __device__ __forceinline__ void operator()(const f32x4 (&acc)[2][2][4][2], const g8::Unit& u, int wr, int wc, int fr, int fq) const {
;         const int row0 = u.pm * 256 + wr * 64 + fr, col0 = u.pn * 256 + wc * 32 + 8 * fq;
; #pragma unroll
;         for (int ai = 0; ai < 2; ++ai)
; #pragma unroll
;             for (int m = 0; m < 4; ++m) { const size_t ro = (size_t)(row0 + ai * 128 + m * 16) * 1024;
; #pragma unroll
;                 for (int bj = 0; bj < 2; ++bj) { const size_t o = ro + col0 + bj * 128;
;                     const u32x4 xb = *(const u32x4*)(XBp + o);
;                     const f32x4 x0 = {__uint_as_float(xb.x << 16), __uint_as_float(xb.x & 0xffff0000u), __uint_as_float(xb.y << 16), __uint_as_float(xb.y & 0xffff0000u)};
;                     const f32x4 x1 = {__uint_as_float(xb.z << 16), __uint_as_float(xb.z & 0xffff0000u), __uint_as_float(xb.w << 16), __uint_as_float(xb.w & 0xffff0000u)};
;                     const f32x4 y0 = x0 * ALPHA + acc[ai][bj][m][0], y1 = x1 * ALPHA + acc[ai][bj][m][1];
;                     *(u32x4*)(Y + o) = (u32x4){cvt_pk_bf16(y0[0], y0[1]), cvt_pk_bf16(y0[2], y0[3]), cvt_pk_bf16(y1[0], y1[1]), cvt_pk_bf16(y1[2], y1[3])}; } }
;     }
	v_lshlrev_b32_e32 v60, 16, v210
	v_and_b32_e32 v61, 0xffff0000, v210
	v_lshlrev_b32_e32 v52, 16, v211
	v_and_b32_e32 v53, 0xffff0000, v211
	v_lshlrev_b32_e32 v62, 16, v212
	v_and_b32_e32 v63, 0xffff0000, v212
	v_lshlrev_b32_e32 v54, 16, v213
	v_and_b32_e32 v55, 0xffff0000, v213
	v_pk_fma_f32 v[50:51], v[52:53], s[24:25], v[50:51] op_sel_hi:[1,0,1]
	v_pk_fma_f32 v[48:49], v[60:61], s[24:25], v[48:49] op_sel_hi:[1,0,1]
	v_pk_fma_f32 v[52:53], v[54:55], s[24:25], v[46:47] op_sel_hi:[1,0,1]
	v_pk_fma_f32 v[46:47], v[62:63], s[24:25], v[44:45] op_sel_hi:[1,0,1]
	v_cvt_pk_bf16_f32 v44, v48, v49
	v_cvt_pk_bf16_f32 v45, v50, v51
	v_cvt_pk_bf16_f32 v46, v46, v47
	v_cvt_pk_bf16_f32 v47, v52, v53
	v_lshl_add_u64 v[48:49], s[14:15], 0, v[56:57]
	global_store_dwordx4 v[48:49], v[44:47], off
	s_waitcnt vmcnt(15)
	v_lshlrev_b32_e32 v50, 16, v214
	v_and_b32_e32 v51, 0xffff0000, v214
	v_lshlrev_b32_e32 v44, 16, v215
	v_and_b32_e32 v45, 0xffff0000, v215
	v_lshlrev_b32_e32 v52, 16, v216
	v_and_b32_e32 v53, 0xffff0000, v216
	v_lshlrev_b32_e32 v46, 16, v217
	v_and_b32_e32 v47, 0xffff0000, v217
	v_pk_fma_f32 v[42:43], v[44:45], s[24:25], v[42:43] op_sel_hi:[1,0,1]
	v_pk_fma_f32 v[40:41], v[50:51], s[24:25], v[40:41] op_sel_hi:[1,0,1]
	v_pk_fma_f32 v[44:45], v[46:47], s[24:25], v[38:39] op_sel_hi:[1,0,1]
	v_pk_fma_f32 v[38:39], v[52:53], s[24:25], v[36:37] op_sel_hi:[1,0,1]
	v_cvt_pk_bf16_f32 v36, v40, v41
	v_cvt_pk_bf16_f32 v37, v42, v43
	v_cvt_pk_bf16_f32 v38, v38, v39
	v_cvt_pk_bf16_f32 v39, v44, v45
	v_lshl_add_u64 v[40:41], v[144:145], 0, s[42:43]
	global_store_dwordx4 v[48:49], v[36:39], off offset:256
	v_lshl_add_u64 v[42:43], s[10:11], 0, v[40:41]
	s_mov_b64 s[42:43], 0x58000
	s_waitcnt vmcnt(15)
	v_lshlrev_b32_e32 v44, 16, v218
	v_and_b32_e32 v45, 0xffff0000, v218
	v_lshlrev_b32_e32 v36, 16, v219
	v_and_b32_e32 v37, 0xffff0000, v219
	v_lshlrev_b32_e32 v46, 16, v220
	v_and_b32_e32 v47, 0xffff0000, v220
	v_lshlrev_b32_e32 v38, 16, v221
	v_and_b32_e32 v39, 0xffff0000, v221
	v_pk_fma_f32 v[34:35], v[36:37], s[24:25], v[34:35] op_sel_hi:[1,0,1]
	v_pk_fma_f32 v[32:33], v[44:45], s[24:25], v[32:33] op_sel_hi:[1,0,1]
	v_pk_fma_f32 v[36:37], v[38:39], s[24:25], v[28:29] op_sel_hi:[1,0,1]
	v_pk_fma_f32 v[28:29], v[46:47], s[24:25], v[26:27] op_sel_hi:[1,0,1]
	v_cvt_pk_bf16_f32 v26, v32, v33
	v_cvt_pk_bf16_f32 v27, v34, v35
	v_cvt_pk_bf16_f32 v28, v28, v29
	v_cvt_pk_bf16_f32 v29, v36, v37
	v_lshl_add_u64 v[32:33], s[14:15], 0, v[40:41]
	global_store_dwordx4 v[32:33], v[26:29], off
	s_waitcnt vmcnt(15)
	v_lshlrev_b32_e32 v34, 16, v222
	v_and_b32_e32 v35, 0xffff0000, v222
	v_lshlrev_b32_e32 v26, 16, v223
	v_and_b32_e32 v27, 0xffff0000, v223
	v_lshlrev_b32_e32 v36, 16, v224
	v_and_b32_e32 v37, 0xffff0000, v224
	v_lshlrev_b32_e32 v28, 16, v225
	v_and_b32_e32 v29, 0xffff0000, v225
	v_pk_fma_f32 v[24:25], v[26:27], s[24:25], v[24:25] op_sel_hi:[1,0,1]
	v_pk_fma_f32 v[22:23], v[34:35], s[24:25], v[22:23] op_sel_hi:[1,0,1]
	v_pk_fma_f32 v[26:27], v[28:29], s[24:25], v[20:21] op_sel_hi:[1,0,1]
	v_pk_fma_f32 v[20:21], v[36:37], s[24:25], v[18:19] op_sel_hi:[1,0,1]
	v_cvt_pk_bf16_f32 v18, v22, v23
	v_cvt_pk_bf16_f32 v19, v24, v25
	v_cvt_pk_bf16_f32 v20, v20, v21
	v_cvt_pk_bf16_f32 v21, v26, v27
	v_lshl_add_u64 v[22:23], v[144:145], 0, s[42:43]
	global_store_dwordx4 v[32:33], v[18:21], off offset:256
	v_lshl_add_u64 v[24:25], s[10:11], 0, v[22:23]
	s_mov_b64 s[42:43], -1
	s_waitcnt vmcnt(15)
	v_lshlrev_b32_e32 v26, 16, v228
	v_and_b32_e32 v27, 0xffff0000, v228
	v_lshlrev_b32_e32 v18, 16, v229
	v_and_b32_e32 v19, 0xffff0000, v229
	v_lshlrev_b32_e32 v28, 16, v230
	v_and_b32_e32 v29, 0xffff0000, v230
	v_lshlrev_b32_e32 v20, 16, v231
	v_and_b32_e32 v21, 0xffff0000, v231
	v_pk_fma_f32 v[16:17], v[18:19], s[24:25], v[16:17] op_sel_hi:[1,0,1]
	v_pk_fma_f32 v[14:15], v[26:27], s[24:25], v[14:15] op_sel_hi:[1,0,1]
	v_pk_fma_f32 v[18:19], v[20:21], s[24:25], v[12:13] op_sel_hi:[1,0,1]
	v_pk_fma_f32 v[12:13], v[28:29], s[24:25], v[10:11] op_sel_hi:[1,0,1]
	v_cvt_pk_bf16_f32 v10, v14, v15
	v_cvt_pk_bf16_f32 v11, v16, v17
	v_cvt_pk_bf16_f32 v12, v12, v13
	v_cvt_pk_bf16_f32 v13, v18, v19
	v_lshl_add_u64 v[14:15], s[14:15], 0, v[22:23]
	global_store_dwordx4 v[14:15], v[10:13], off
	s_waitcnt vmcnt(15)
	v_lshlrev_b32_e32 v16, 16, v232
	v_and_b32_e32 v17, 0xffff0000, v232
	v_lshlrev_b32_e32 v10, 16, v233
	v_and_b32_e32 v11, 0xffff0000, v233
	v_lshlrev_b32_e32 v18, 16, v234
	v_and_b32_e32 v19, 0xffff0000, v234
	v_lshlrev_b32_e32 v12, 16, v235
	v_and_b32_e32 v13, 0xffff0000, v235
	v_pk_fma_f32 v[8:9], v[10:11], s[24:25], v[8:9] op_sel_hi:[1,0,1]
	v_pk_fma_f32 v[6:7], v[16:17], s[24:25], v[6:7] op_sel_hi:[1,0,1]
	v_pk_fma_f32 v[10:11], v[12:13], s[24:25], v[4:5] op_sel_hi:[1,0,1]
	v_pk_fma_f32 v[4:5], v[18:19], s[24:25], v[2:3] op_sel_hi:[1,0,1]
	v_cvt_pk_bf16_f32 v2, v6, v7
	v_cvt_pk_bf16_f32 v3, v8, v9
	v_cvt_pk_bf16_f32 v4, v4, v5
	v_cvt_pk_bf16_f32 v5, v10, v11
	global_store_dwordx4 v[14:15], v[2:5], off offset:256
	s_cbranch_vccnz .LBB0_1276
	s_and_b64 vcc, exec, s[38:39]
	s_cbranch_vccnz .LBB0_1275
	s_barrier
	s_branch .LBB0_1275
